# LayerNorm bf16 output packs: v_cvt_pk_bf16_f32 instead of the 7-instruction RNE bit trick (40 pairs)
# baseline (speedup 1.0000x reference)
; template <bool ROUTE, bool COMBINE> ...
;     f32x4 v[8]; float s = 0.f;
;     if (!COMBINE) {
;         if (pre) {
; #pragma unroll
;             for (int j = 0; j < 4; ++j) bf8_to_f32(pre[j], v[2 * j], v[2 * j + 1]);
;         } else {
;             const bf16* yr = Yb + (size_t)row * D_ + 8 * lane;
; #pragma unroll
;             for (int j = 0; j < 4; ++j) bf8_to_f32(*(const u32x4*)(yr + 512 * j), v[2 * j], v[2 * j + 1]);
;         }
;     } else {
;         const int p0 = pos[row * 2], p1 = pos[row * 2 + 1]; const float g0 = topg[row * 2], g1 = topg[row * 2 + 1];
; #pragma unroll
;         for (int j = 0; j < 4; ++j) { const int c = 8 * lane + 512 * j;
;             f32x4 xa, xb, pa, pb, a0, a1, c0, c1;
;             bf8_to_f32(*(const u32x4*)(X1B + (size_t)row * D_ + c), xa, xb); bf8_to_f32(*(const u32x4*)(PLEB + (size_t)row * D_ + c), pa, pb);
;             bf8_to_f32(*(const u32x4*)(YE + (size_t)p0 * D_ + c), a0, a1);
;             bf8_to_f32(*(const u32x4*)(YE + (size_t)p1 * D_ + c), c0, c1);
;             v[2 * j] = (ALPHA * xa + (g0 * a0 + g1 * c0)) + pa; v[2 * j + 1] = (ALPHA * xb + (g0 * a1 + g1 * c1)) + pb; }
;     }
; #pragma unroll
;     for (int j = 0; j < 8; ++j) s += (v[j].x + v[j].y) + (v[j].z + v[j].w);
;     const float mean = wave_sum(s) * (1.0f / D_); float s2 = 0.f;
; #pragma unroll
;     for (int j = 0; j < 8; ++j) { v[j] = v[j] - mean; s2 += (v[j].x * v[j].x + v[j].y * v[j].y) + (v[j].z * v[j].z + v[j].w * v[j].w); }
;     const float rstd = 1.0f / sqrtf(wave_sum(s2) * (1.0f / D_) + LN_EPS);
.LBB0_633:
	s_waitcnt vmcnt(17)
	v_lshlrev_b32_e32 v119, 16, v88
	v_lshlrev_b32_e32 v118, 16, v90
	v_and_b32_e32 v121, 0xffff0000, v88
	v_and_b32_e32 v120, 0xffff0000, v90
	v_lshlrev_b32_e32 v115, 16, v89
	v_lshlrev_b32_e32 v114, 16, v91
	v_and_b32_e32 v117, 0xffff0000, v89
	v_and_b32_e32 v116, 0xffff0000, v91
	v_pk_add_f32 v[88:89], v[118:119], v[120:121]
	v_pk_add_f32 v[90:91], v[114:115], v[116:117]
	v_lshlrev_b32_e32 v102, 16, v81
	v_pk_add_f32 v[88:89], v[88:89], v[90:91]
	v_and_b32_e32 v106, 0xffff0000, v81
	v_add_f32_e32 v81, 0, v89
	v_add_f32_e32 v107, v88, v81
	v_lshlrev_b32_e32 v89, 16, v85
	v_lshlrev_b32_e32 v88, 16, v84
	v_and_b32_e32 v91, 0xffff0000, v85
	v_and_b32_e32 v90, 0xffff0000, v84
	v_pk_add_f32 v[84:85], v[88:89], v[90:91]
	v_lshlrev_b32_e32 v110, 16, v86
	v_and_b32_e32 v111, 0xffff0000, v86
	v_lshlrev_b32_e32 v112, 16, v87
	v_and_b32_e32 v113, 0xffff0000, v87
	v_pk_add_f32 v[84:85], v[84:85], v[84:85] op_sel_hi:[0,1]
	v_lshlrev_b32_e32 v104, 16, v80
	v_and_b32_e32 v108, 0xffff0000, v80
	v_add_f32_e32 v105, v110, v111
	v_add_f32_e32 v109, v112, v113
	v_mov_b32_e32 v103, v85
	v_pk_add_f32 v[130:131], v[104:105], v[108:109]
	v_pk_add_f32 v[84:85], v[102:103], v[106:107]
	s_waitcnt vmcnt(16)
	v_lshlrev_b32_e32 v98, 16, v92
	v_pk_add_f32 v[84:85], v[130:131], v[84:85]
	v_and_b32_e32 v99, 0xffff0000, v92
	v_pk_add_f32 v[130:131], v[84:85], v[84:85] op_sel_hi:[0,1]
	v_lshlrev_b32_e32 v85, 16, v83
	v_lshlrev_b32_e32 v84, 16, v82
	v_and_b32_e32 v83, 0xffff0000, v83
	v_and_b32_e32 v82, 0xffff0000, v82
	v_pk_add_f32 v[132:133], v[84:85], v[82:83]
	v_lshlrev_b32_e32 v100, 16, v93
	v_and_b32_e32 v101, 0xffff0000, v93
	v_pk_add_f32 v[132:133], v[132:133], v[132:133] op_sel_hi:[0,1]
	v_lshlrev_b32_e32 v86, 16, v94
	v_and_b32_e32 v94, 0xffff0000, v94
	v_lshlrev_b32_e32 v80, 16, v95
	v_and_b32_e32 v92, 0xffff0000, v95
	v_add_f32_e32 v87, v98, v99
	v_add_f32_e32 v95, v100, v101
	v_mov_b32_e32 v81, v133
	v_mov_b32_e32 v93, v131
	v_pk_add_f32 v[134:135], v[86:87], v[94:95]
	v_pk_add_f32 v[130:131], v[80:81], v[92:93]
	s_nop 0
	v_pk_add_f32 v[130:131], v[134:135], v[130:131]
	s_nop 0
	v_add_f32_e32 v81, v130, v131
	ds_bpermute_b32 v87, v122, v81
	s_waitcnt lgkmcnt(0)
	v_add_f32_e32 v81, v81, v87
	ds_bpermute_b32 v87, v123, v81
	s_waitcnt lgkmcnt(0)
	v_add_f32_e32 v81, v81, v87
	ds_bpermute_b32 v87, v124, v81
	s_waitcnt lgkmcnt(0)
	v_add_f32_e32 v81, v81, v87
	ds_bpermute_b32 v87, v125, v81
	s_waitcnt lgkmcnt(0)
	v_add_f32_e32 v81, v81, v87
	ds_bpermute_b32 v87, v126, v81
	s_waitcnt lgkmcnt(0)
	v_add_f32_e32 v81, v81, v87
	ds_bpermute_b32 v87, v127, v81
	s_waitcnt lgkmcnt(0)
	v_add_f32_e32 v81, v81, v87
	v_fmac_f32_e32 v121, 0xba000000, v81
	v_fmac_f32_e32 v120, 0xba000000, v81
	v_fmac_f32_e32 v117, 0xba000000, v81
	v_fmac_f32_e32 v119, 0xba000000, v81
	v_fmac_f32_e32 v116, 0xba000000, v81
	v_fmac_f32_e32 v118, 0xba000000, v81
	v_mov_b32_e32 v132, v121
	v_mov_b32_e32 v133, v120
	v_fmac_f32_e32 v115, 0xba000000, v81
	v_fmac_f32_e32 v114, 0xba000000, v81
	v_mov_b32_e32 v130, v119
	v_mov_b32_e32 v131, v118
	v_pk_mul_f32 v[132:133], v[132:133], v[132:133]
	v_mov_b32_e32 v134, v117
	v_mov_b32_e32 v135, v116
	v_pk_fma_f32 v[130:131], v[130:131], v[130:131], v[132:133]
	v_mov_b32_e32 v132, v115
	v_mov_b32_e32 v133, v114
	v_pk_mul_f32 v[134:135], v[134:135], v[134:135]
	v_fmac_f32_e32 v90, 0xba000000, v81
	v_pk_fma_f32 v[132:133], v[132:133], v[132:133], v[134:135]
	v_fmac_f32_e32 v91, 0xba000000, v81
	v_fmac_f32_e32 v89, 0xba000000, v81
	v_pk_add_f32 v[130:131], v[130:131], v[132:133]
	v_fmac_f32_e32 v88, 0xba000000, v81
	v_mov_b32_e32 v132, v89
	v_mov_b32_e32 v133, v91
	v_mov_b32_e32 v89, v90
	v_pk_mul_f32 v[134:135], v[132:133], v[132:133]
	v_pk_mul_f32 v[90:91], v[88:89], v[88:89]
	v_fmac_f32_e32 v110, 0xba000000, v81
	v_pk_mov_b32 v[136:137], v[90:91], v[134:135] op_sel:[1,0]
	v_mov_b32_e32 v91, v135
	v_pk_add_f32 v[90:91], v[136:137], v[90:91]
	v_fmac_f32_e32 v111, 0xba000000, v81
	v_pk_add_f32 v[90:91], v[90:91], v[90:91] op_sel_hi:[0,1]
	v_fmac_f32_e32 v112, 0xba000000, v81
	v_mul_f32_e32 v90, v110, v110
	v_fmac_f32_e32 v113, 0xba000000, v81
	v_pk_fma_f32 v[134:135], v[110:111], v[110:111], v[90:91] op_sel_hi:[1,1,0]
	v_mul_f32_e32 v90, v112, v112
	v_pk_add_f32 v[130:131], v[130:131], v[130:131] op_sel_hi:[0,1]
	v_pk_fma_f32 v[136:137], v[112:113], v[112:113], v[90:91] op_sel_hi:[1,1,0]
	v_fmac_f32_e32 v106, 0xba000000, v81
	v_fmac_f32_e32 v102, 0xba000000, v81
	v_fmac_f32_e32 v108, 0xba000000, v81
	v_fmac_f32_e32 v104, 0xba000000, v81
	v_mul_f32_e32 v134, v104, v104
	v_mul_f32_e32 v136, v108, v108
	v_mul_f32_e32 v90, v102, v102
	v_mul_f32_e32 v130, v106, v106
	v_fmac_f32_e32 v82, 0xba000000, v81
	v_fmac_f32_e32 v83, 0xba000000, v81
	v_fmac_f32_e32 v85, 0xba000000, v81
	v_pk_add_f32 v[134:135], v[134:135], v[136:137]
	v_pk_add_f32 v[90:91], v[90:91], v[130:131]
	v_fmac_f32_e32 v84, 0xba000000, v81
	v_mov_b32_e32 v130, v85
	v_mov_b32_e32 v131, v83
	v_mov_b32_e32 v85, v82
	v_pk_add_f32 v[90:91], v[134:135], v[90:91]
	v_pk_mul_f32 v[134:135], v[130:131], v[130:131]
	v_pk_mul_f32 v[82:83], v[84:85], v[84:85]
	v_fmac_f32_e32 v98, 0xba000000, v81
	v_pk_mov_b32 v[136:137], v[82:83], v[134:135] op_sel:[1,0]
	v_mov_b32_e32 v83, v135
	v_pk_add_f32 v[82:83], v[136:137], v[82:83]
	v_fmac_f32_e32 v99, 0xba000000, v81
	v_pk_add_f32 v[82:83], v[82:83], v[82:83] op_sel_hi:[0,1]
	v_fmac_f32_e32 v100, 0xba000000, v81
	v_mul_f32_e32 v82, v98, v98
	v_fmac_f32_e32 v101, 0xba000000, v81
	v_pk_fma_f32 v[134:135], v[98:99], v[98:99], v[82:83] op_sel_hi:[1,1,0]
	v_mul_f32_e32 v82, v100, v100
	v_pk_add_f32 v[90:91], v[90:91], v[90:91] op_sel_hi:[0,1]
	v_pk_fma_f32 v[136:137], v[100:101], v[100:101], v[82:83] op_sel_hi:[1,1,0]
	v_fmac_f32_e32 v92, 0xba000000, v81
	v_fmac_f32_e32 v80, 0xba000000, v81
	v_fmac_f32_e32 v94, 0xba000000, v81
	v_fmac_f32_e32 v86, 0xba000000, v81
	v_mul_f32_e32 v134, v86, v86
	v_mul_f32_e32 v136, v94, v94
	v_mul_f32_e32 v82, v80, v80
	v_mul_f32_e32 v90, v92, v92
	v_pk_add_f32 v[134:135], v[134:135], v[136:137]
	v_pk_add_f32 v[82:83], v[82:83], v[90:91]
	v_mov_b32_e32 v90, v114
	v_pk_add_f32 v[82:83], v[134:135], v[82:83]
	s_nop 0
	v_add_f32_e32 v81, v82, v83
	ds_bpermute_b32 v82, v122, v81
	v_mov_b32_e32 v83, v120
	v_mov_b32_e32 v120, v119
	s_waitcnt lgkmcnt(0)
; DI unsigned f2bf(float f) { unsigned u = __builtin_bit_cast(unsigned, f); return (u + 0x7fffu + ((u >> 16) & 1u)) >> 16; }
; template <bool ROUTE, bool COMBINE> ...
;     ...
;     const float rstd = 1.0f / sqrtf(wave_sum(s2) * (1.0f / D_) + LN_EPS);
;     float lg0 = 0.f, lg1 = 0.f, lg2 = 0.f, lg3 = 0.f, lg4 = 0.f, lg5 = 0.f, lg6 = 0.f, lg7 = 0.f;
; #pragma unroll
;     for (int j = 0; j < 4; ++j) {
;         const int c = 8 * lane + 512 * j;
;         const f32x4 oa = v[2 * j] * rstd * *(const f32x4*)(g + c) + *(const f32x4*)(bta + c), ob = v[2 * j + 1] * rstd * *(const f32x4*)(g + c + 4) + *(const f32x4*)(bta + c + 4);
;         if (X) { *(f32x4*)(X + (size_t)row * D_ + c) = oa; *(f32x4*)(X + (size_t)row * D_ + c + 4) = ob; }
;         if (XB) { u32x4 w; w.x = f2bf(oa.x) | (f2bf(oa.y) << 16); w.y = f2bf(oa.z) | (f2bf(oa.w) << 16); w.z = f2bf(ob.x) | (f2bf(ob.y) << 16); w.w = f2bf(ob.z) | (f2bf(ob.w) << 16);
;             *(u32x4*)(XB + (size_t)row * D_ + c) = w; }
	v_add_f32_e32 v81, v81, v82
	ds_bpermute_b32 v82, v123, v81
	s_waitcnt lgkmcnt(0)
	v_add_f32_e32 v81, v81, v82
	ds_bpermute_b32 v82, v124, v81
	s_waitcnt lgkmcnt(0)
	v_add_f32_e32 v81, v81, v82
	ds_bpermute_b32 v82, v125, v81
	s_waitcnt lgkmcnt(0)
	v_add_f32_e32 v81, v81, v82
	ds_bpermute_b32 v82, v126, v81
	s_waitcnt lgkmcnt(0)
	v_add_f32_e32 v81, v81, v82
	ds_bpermute_b32 v87, v127, v81
	v_mov_b32_e32 v82, v118
	s_waitcnt lgkmcnt(0)
	v_add_f32_e32 v81, v81, v87
	v_fmamk_f32 v81, v81, 0x3a000000, v128
	v_mul_f32_e32 v87, 0x4f800000, v81
	v_cmp_gt_f32_e32 vcc, s9, v81
	s_nop 1
	v_cndmask_b32_e32 v81, v81, v87, vcc
	v_sqrt_f32_e32 v87, v81
	s_nop 0
	v_add_u32_e32 v91, -1, v87
	v_fma_f32 v93, -v91, v87, v81
	v_cmp_ge_f32_e64 s[4:5], 0, v93
	v_add_u32_e32 v93, 1, v87
	s_nop 0
	v_cndmask_b32_e64 v91, v87, v91, s[4:5]
	v_fma_f32 v87, -v93, v87, v81
	v_cmp_lt_f32_e64 s[4:5], 0, v87
	s_nop 1
	v_cndmask_b32_e64 v87, v91, v93, s[4:5]
	v_mul_f32_e32 v91, 0x37800000, v87
	v_cndmask_b32_e32 v87, v87, v91, vcc
	v_cmp_class_f32_e32 vcc, v81, v129
	v_mov_b32_e32 v91, v116
	v_mov_b32_e32 v116, v115
	v_cndmask_b32_e32 v81, v87, v81, vcc
	v_div_scale_f32 v87, s[4:5], v81, v81, 1.0
	v_rcp_f32_e32 v93, v87
	s_nop 0
	v_fma_f32 v95, -v87, v93, 1.0
	v_fmac_f32_e32 v93, v95, v93
	v_div_scale_f32 v95, vcc, 1.0, v81, 1.0
	v_mul_f32_e32 v103, v95, v93
	v_fma_f32 v105, -v87, v103, v95
	v_fmac_f32_e32 v103, v105, v93
	v_fma_f32 v87, -v87, v103, v95
	v_div_fmas_f32 v87, v87, v93, v103
	v_div_fixup_f32 v118, v87, v81, 1.0
	v_pk_mul_f32 v[114:115], v[120:121], v[118:119] op_sel_hi:[1,0]
	v_pk_mul_f32 v[116:117], v[116:117], v[118:119] op_sel_hi:[1,0]
	s_waitcnt vmcnt(12)
	v_pk_fma_f32 v[114:115], v[4:5], v[114:115], v[12:13]
	v_pk_fma_f32 v[116:117], v[6:7], v[116:117], v[14:15]
	v_cvt_pk_bf16_f32 v114, v114, v115
	v_pk_mul_f32 v[82:83], v[82:83], v[118:119] op_sel_hi:[1,0]
	v_pk_fma_f32 v[82:83], v[0:1], v[82:83], v[8:9]
	v_cvt_pk_bf16_f32 v115, v116, v117
	v_bfe_u32 v81, v82, 16, 1
	v_pk_mul_f32 v[90:91], v[90:91], v[118:119] op_sel_hi:[1,0]
	v_add3_u32 v81, v82, v81, s18
	v_bfe_u32 v82, v83, 16, 1
	v_pk_fma_f32 v[90:91], v[2:3], v[90:91], v[10:11]
	v_lshrrev_b32_e32 v81, 16, v81
	v_add3_u32 v82, v83, v82, s18
	v_and_or_b32 v116, v82, s3, v81
	v_cvt_pk_bf16_f32 v117, v90, v91
	v_lshl_add_u64 v[82:83], s[10:11], 0, v[96:97]
	v_add_co_u32_e32 v120, vcc, s19, v82
	v_mov_b32_e32 v105, v108
	s_nop 0
	v_addc_co_u32_e32 v121, vcc, 0, v83, vcc
	v_pk_mul_f32 v[82:83], v[88:89], v[118:119] op_sel_hi:[1,0]
	v_pk_mul_f32 v[88:89], v[132:133], v[118:119] op_sel_hi:[1,0]
	s_waitcnt vmcnt(8)
	v_pk_fma_f32 v[82:83], v[20:21], v[82:83], v[28:29]
	v_pk_fma_f32 v[90:91], v[22:23], v[88:89], v[30:31]
	v_bfe_u32 v81, v82, 16, 1
	v_add3_u32 v81, v82, v81, s18
	v_bfe_u32 v82, v83, 16, 1
	v_pk_mul_f32 v[88:89], v[110:111], v[118:119] op_sel_hi:[1,0]
	v_lshrrev_b32_e32 v81, 16, v81
	v_add3_u32 v82, v83, v82, s18
	v_pk_mul_f32 v[110:111], v[112:113], v[118:119] op_sel_hi:[1,0]
	v_pk_fma_f32 v[112:113], v[16:17], v[88:89], v[24:25]
	v_and_or_b32 v88, v82, s3, v81
	v_cvt_pk_bf16_f32 v89, v90, v91
	v_pk_fma_f32 v[110:111], v[18:19], v[110:111], v[26:27]
	v_cvt_pk_bf16_f32 v90, v112, v113
	v_bfe_u32 v81, v110, 16, 1
	v_add3_u32 v81, v110, v81, s18
	v_bfe_u32 v82, v111, 16, 1
	v_lshrrev_b32_e32 v81, 16, v81
	v_add3_u32 v82, v111, v82, s18
	v_and_or_b32 v91, v82, s3, v81
	v_pk_mul_f32 v[82:83], v[104:105], v[118:119] op_sel_hi:[1,0]
	v_mov_b32_e32 v103, v106
	s_waitcnt vmcnt(4)
	v_pk_fma_f32 v[82:83], v[36:37], v[82:83], v[44:45]
	global_store_dwordx4 v[120:121], v[88:91], off offset:1024
	v_bfe_u32 v81, v82, 16, 1
	v_add3_u32 v81, v82, v81, s18
	v_pk_mul_f32 v[88:89], v[102:103], v[118:119] op_sel_hi:[1,0]
	v_bfe_u32 v82, v83, 16, 1
	v_pk_fma_f32 v[88:89], v[38:39], v[88:89], v[46:47]
	v_lshrrev_b32_e32 v81, 16, v81
	v_add3_u32 v82, v83, v82, s18
	v_and_or_b32 v82, v82, s3, v81
	v_pk_mul_f32 v[84:85], v[84:85], v[118:119] op_sel_hi:[1,0]
	v_pk_fma_f32 v[84:85], v[32:33], v[84:85], v[40:41]
	v_cvt_pk_bf16_f32 v83, v88, v89
	v_bfe_u32 v81, v84, 16, 1
	v_pk_mul_f32 v[90:91], v[130:131], v[118:119] op_sel_hi:[1,0]
	v_add3_u32 v81, v84, v81, s18
	v_bfe_u32 v84, v85, 16, 1
	v_pk_fma_f32 v[90:91], v[34:35], v[90:91], v[42:43]
	v_lshrrev_b32_e32 v81, 16, v81
	v_add3_u32 v84, v85, v84, s18
	v_and_or_b32 v84, v84, s3, v81
	v_cvt_pk_bf16_f32 v85, v90, v91
	global_store_dwordx4 v[120:121], v[82:85], off offset:2048
	v_mov_b32_e32 v81, v92
	v_pk_mul_f32 v[80:81], v[80:81], v[118:119] op_sel_hi:[1,0]
	v_pk_mul_f32 v[82:83], v[98:99], v[118:119] op_sel_hi:[1,0]
	s_waitcnt vmcnt(3)
	v_pk_fma_f32 v[88:89], v[50:51], v[80:81], v[58:59]
	s_waitcnt vmcnt(2)
	v_pk_fma_f32 v[82:83], v[52:53], v[82:83], v[60:61]
	v_pk_mul_f32 v[84:85], v[100:101], v[118:119] op_sel_hi:[1,0]
	v_pk_fma_f32 v[84:85], v[54:55], v[84:85], v[62:63]
	v_mov_b32_e32 v87, v94
	v_cvt_pk_bf16_f32 v80, v82, v83
	v_pk_mul_f32 v[86:87], v[86:87], v[118:119] op_sel_hi:[1,0]
	v_pk_fma_f32 v[86:87], v[48:49], v[86:87], v[56:57]
	v_cvt_pk_bf16_f32 v81, v84, v85
	v_cvt_pk_bf16_f32 v82, v86, v87
	s_add_u32 s10, s10, s12
	s_addc_u32 s11, s11, s13
	v_cvt_pk_bf16_f32 v83, v88, v89
	s_add_u32 s14, s14, s12
	global_store_dwordx4 v[120:121], v[80:83], off offset:3072
	s_addc_u32 s15, s15, s13
	s_andn2_b64 vcc, exec, s[16:17]
	v_mov_b32_e32 v92, v76
	v_mov_b32_e32 v93, v77
	v_mov_b32_e32 v94, v78
	v_mov_b32_e32 v95, v79
	v_mov_b32_e32 v80, v72
	v_mov_b32_e32 v81, v73
	v_mov_b32_e32 v82, v74
	v_mov_b32_e32 v83, v75
	v_mov_b32_e32 v84, v68
	v_mov_b32_e32 v85, v69
	v_mov_b32_e32 v86, v70
	v_mov_b32_e32 v87, v71
	v_mov_b32_e32 v88, v64
	v_mov_b32_e32 v89, v65
	v_mov_b32_e32 v90, v66
	v_mov_b32_e32 v91, v67
	global_store_dwordx4 v[120:121], v[114:117], off
	s_cbranch_vccz .LBB0_636

; template <bool ROUTE, bool COMBINE> ...
;     f32x4 v[8]; float s = 0.f;
;     if (!COMBINE) {
;         if (pre) {
; #pragma unroll
;             for (int j = 0; j < 4; ++j) bf8_to_f32(pre[j], v[2 * j], v[2 * j + 1]);
;         } else {
;             const bf16* yr = Yb + (size_t)row * D_ + 8 * lane;
; #pragma unroll
;             for (int j = 0; j < 4; ++j) bf8_to_f32(*(const u32x4*)(yr + 512 * j), v[2 * j], v[2 * j + 1]);
;         }
;     } else {
;         const int p0 = pos[row * 2], p1 = pos[row * 2 + 1]; const float g0 = topg[row * 2], g1 = topg[row * 2 + 1];
; #pragma unroll
;         for (int j = 0; j < 4; ++j) { const int c = 8 * lane + 512 * j;
;             f32x4 xa, xb, pa, pb, a0, a1, c0, c1;
;             bf8_to_f32(*(const u32x4*)(X1B + (size_t)row * D_ + c), xa, xb); bf8_to_f32(*(const u32x4*)(PLEB + (size_t)row * D_ + c), pa, pb);
;             bf8_to_f32(*(const u32x4*)(YE + (size_t)p0 * D_ + c), a0, a1);
;             bf8_to_f32(*(const u32x4*)(YE + (size_t)p1 * D_ + c), c0, c1);
;             v[2 * j] = (ALPHA * xa + (g0 * a0 + g1 * c0)) + pa; v[2 * j + 1] = (ALPHA * xb + (g0 * a1 + g1 * c1)) + pb; }
;     }
; #pragma unroll
;     for (int j = 0; j < 8; ++j) s += (v[j].x + v[j].y) + (v[j].z + v[j].w);
;     const float mean = wave_sum(s) * (1.0f / D_); float s2 = 0.f;
; #pragma unroll
;     for (int j = 0; j < 8; ++j) { v[j] = v[j] - mean; s2 += (v[j].x * v[j].x + v[j].y * v[j].y) + (v[j].z * v[j].z + v[j].w * v[j].w); }
;     const float rstd = 1.0f / sqrtf(wave_sum(s2) * (1.0f / D_) + LN_EPS);
.LBB0_873:
	s_waitcnt vmcnt(17)
	v_lshlrev_b32_e32 v123, 16, v88
	v_lshlrev_b32_e32 v122, 16, v90
	v_and_b32_e32 v125, 0xffff0000, v88
	v_and_b32_e32 v124, 0xffff0000, v90
	v_lshlrev_b32_e32 v119, 16, v89
	v_lshlrev_b32_e32 v118, 16, v91
	v_and_b32_e32 v121, 0xffff0000, v89
	v_and_b32_e32 v120, 0xffff0000, v91
	v_pk_add_f32 v[88:89], v[122:123], v[124:125]
	v_pk_add_f32 v[90:91], v[118:119], v[120:121]
	v_lshlrev_b32_e32 v106, 16, v81
	v_pk_add_f32 v[88:89], v[88:89], v[90:91]
	v_and_b32_e32 v110, 0xffff0000, v81
	v_add_f32_e32 v81, 0, v89
	v_add_f32_e32 v111, v88, v81
	v_lshlrev_b32_e32 v89, 16, v85
	v_lshlrev_b32_e32 v88, 16, v84
	v_and_b32_e32 v91, 0xffff0000, v85
	v_and_b32_e32 v90, 0xffff0000, v84
	v_pk_add_f32 v[84:85], v[88:89], v[90:91]
	v_lshlrev_b32_e32 v114, 16, v86
	v_and_b32_e32 v115, 0xffff0000, v86
	v_lshlrev_b32_e32 v116, 16, v87
	v_and_b32_e32 v117, 0xffff0000, v87
	v_pk_add_f32 v[84:85], v[84:85], v[84:85] op_sel_hi:[0,1]
	v_lshlrev_b32_e32 v108, 16, v80
	v_and_b32_e32 v112, 0xffff0000, v80
	v_add_f32_e32 v109, v114, v115
	v_add_f32_e32 v113, v116, v117
	v_mov_b32_e32 v107, v85
	v_pk_add_f32 v[136:137], v[108:109], v[112:113]
	v_pk_add_f32 v[84:85], v[106:107], v[110:111]
	v_and_b32_e32 v139, 0xffff0000, v83
	v_pk_add_f32 v[84:85], v[136:137], v[84:85]
	v_and_b32_e32 v138, 0xffff0000, v82
	v_pk_add_f32 v[136:137], v[84:85], v[84:85] op_sel_hi:[0,1]
	v_lshlrev_b32_e32 v85, 16, v83
	v_lshlrev_b32_e32 v84, 16, v82
	v_pk_add_f32 v[82:83], v[84:85], v[138:139]
	s_waitcnt vmcnt(16)
	v_lshlrev_b32_e32 v102, 16, v92
	v_and_b32_e32 v103, 0xffff0000, v92
	v_lshlrev_b32_e32 v104, 16, v93
	v_and_b32_e32 v105, 0xffff0000, v93
	v_pk_add_f32 v[82:83], v[82:83], v[82:83] op_sel_hi:[0,1]
	v_lshlrev_b32_e32 v86, 16, v94
	v_and_b32_e32 v94, 0xffff0000, v94
	v_lshlrev_b32_e32 v80, 16, v95
	v_and_b32_e32 v92, 0xffff0000, v95
	v_add_f32_e32 v87, v102, v103
	v_add_f32_e32 v95, v104, v105
	v_mov_b32_e32 v81, v83
	v_mov_b32_e32 v93, v137
	v_pk_add_f32 v[140:141], v[86:87], v[94:95]
	v_pk_add_f32 v[82:83], v[80:81], v[92:93]
	v_lshl_add_u64 v[100:101], v[100:101], 0, s[14:15]
	v_pk_add_f32 v[82:83], v[140:141], v[82:83]
	s_nop 0
	v_add_f32_e32 v81, v82, v83
	ds_bpermute_b32 v82, v126, v81
	s_waitcnt lgkmcnt(0)
	v_add_f32_e32 v81, v81, v82
	ds_bpermute_b32 v82, v127, v81
	s_waitcnt lgkmcnt(0)
	v_add_f32_e32 v81, v81, v82
	ds_bpermute_b32 v82, v128, v81
	s_waitcnt lgkmcnt(0)
	v_add_f32_e32 v81, v81, v82
	ds_bpermute_b32 v82, v129, v81
	s_waitcnt lgkmcnt(0)
	v_add_f32_e32 v81, v81, v82
	ds_bpermute_b32 v82, v130, v81
	s_waitcnt lgkmcnt(0)
	v_add_f32_e32 v81, v81, v82
	ds_bpermute_b32 v82, v131, v81
	s_waitcnt lgkmcnt(0)
	v_add_f32_e32 v81, v81, v82
	v_fmac_f32_e32 v125, 0xba000000, v81
	v_fmac_f32_e32 v124, 0xba000000, v81
	v_fmac_f32_e32 v121, 0xba000000, v81
	v_fmac_f32_e32 v123, 0xba000000, v81
	v_fmac_f32_e32 v120, 0xba000000, v81
	v_fmac_f32_e32 v122, 0xba000000, v81
	v_mov_b32_e32 v136, v125
	v_mov_b32_e32 v137, v124
	v_fmac_f32_e32 v119, 0xba000000, v81
	v_fmac_f32_e32 v118, 0xba000000, v81
	v_mov_b32_e32 v82, v123
	v_mov_b32_e32 v83, v122
	v_pk_mul_f32 v[136:137], v[136:137], v[136:137]
	v_mov_b32_e32 v140, v121
	v_mov_b32_e32 v141, v120
	v_pk_fma_f32 v[82:83], v[82:83], v[82:83], v[136:137]
	v_mov_b32_e32 v136, v119
	v_mov_b32_e32 v137, v118
	v_pk_mul_f32 v[140:141], v[140:141], v[140:141]
	v_fmac_f32_e32 v90, 0xba000000, v81
	v_pk_fma_f32 v[136:137], v[136:137], v[136:137], v[140:141]
	v_fmac_f32_e32 v91, 0xba000000, v81
	v_fmac_f32_e32 v89, 0xba000000, v81
	v_pk_add_f32 v[82:83], v[82:83], v[136:137]
	v_fmac_f32_e32 v88, 0xba000000, v81
	v_mov_b32_e32 v136, v89
	v_mov_b32_e32 v137, v91
	v_mov_b32_e32 v89, v90
	v_pk_add_f32 v[82:83], v[82:83], v[82:83] op_sel_hi:[0,1]
	v_pk_mul_f32 v[140:141], v[136:137], v[136:137]
	v_pk_mul_f32 v[90:91], v[88:89], v[88:89]
	v_fmac_f32_e32 v114, 0xba000000, v81
	v_pk_mov_b32 v[142:143], v[90:91], v[140:141] op_sel:[1,0]
	v_mov_b32_e32 v91, v141
	v_fmac_f32_e32 v115, 0xba000000, v81
	v_fmac_f32_e32 v116, 0xba000000, v81
	v_mul_f32_e32 v82, v114, v114
	v_pk_add_f32 v[90:91], v[142:143], v[90:91]
	v_fmac_f32_e32 v117, 0xba000000, v81
	v_pk_fma_f32 v[140:141], v[114:115], v[114:115], v[82:83] op_sel_hi:[1,1,0]
	v_mul_f32_e32 v82, v116, v116
	v_pk_add_f32 v[90:91], v[90:91], v[90:91] op_sel_hi:[0,1]
	v_pk_fma_f32 v[142:143], v[116:117], v[116:117], v[82:83] op_sel_hi:[1,1,0]
	v_fmac_f32_e32 v110, 0xba000000, v81
	v_fmac_f32_e32 v106, 0xba000000, v81
	v_fmac_f32_e32 v112, 0xba000000, v81
	v_fmac_f32_e32 v108, 0xba000000, v81
	v_mul_f32_e32 v140, v108, v108
	v_mul_f32_e32 v142, v112, v112
	v_mul_f32_e32 v90, v106, v106
	v_mul_f32_e32 v82, v110, v110
	v_pk_add_f32 v[140:141], v[140:141], v[142:143]
	v_pk_add_f32 v[82:83], v[90:91], v[82:83]
	v_fmac_f32_e32 v138, 0xba000000, v81
	v_pk_add_f32 v[82:83], v[140:141], v[82:83]
	v_fmac_f32_e32 v139, 0xba000000, v81
	v_fmac_f32_e32 v85, 0xba000000, v81
	v_pk_add_f32 v[90:91], v[82:83], v[82:83] op_sel_hi:[0,1]
	v_fmac_f32_e32 v84, 0xba000000, v81
	v_mov_b32_e32 v82, v85
	v_mov_b32_e32 v83, v139
	v_mov_b32_e32 v85, v138
	v_pk_mul_f32 v[140:141], v[82:83], v[82:83]
	v_pk_mul_f32 v[138:139], v[84:85], v[84:85]
	v_fmac_f32_e32 v102, 0xba000000, v81
	v_pk_mov_b32 v[142:143], v[138:139], v[140:141] op_sel:[1,0]
	v_mov_b32_e32 v139, v141
	v_fmac_f32_e32 v103, 0xba000000, v81
	v_fmac_f32_e32 v104, 0xba000000, v81
	v_mul_f32_e32 v90, v102, v102
	v_pk_add_f32 v[138:139], v[142:143], v[138:139]
	v_fmac_f32_e32 v105, 0xba000000, v81
	v_pk_fma_f32 v[140:141], v[102:103], v[102:103], v[90:91] op_sel_hi:[1,1,0]
	v_mul_f32_e32 v90, v104, v104
	v_pk_add_f32 v[138:139], v[138:139], v[138:139] op_sel_hi:[0,1]
	v_pk_fma_f32 v[142:143], v[104:105], v[104:105], v[90:91] op_sel_hi:[1,1,0]
	v_fmac_f32_e32 v92, 0xba000000, v81
	v_fmac_f32_e32 v80, 0xba000000, v81
	v_fmac_f32_e32 v94, 0xba000000, v81
	v_fmac_f32_e32 v86, 0xba000000, v81
	v_mul_f32_e32 v140, v86, v86
	v_mul_f32_e32 v142, v94, v94
	v_mul_f32_e32 v138, v80, v80
	v_mul_f32_e32 v90, v92, v92
	v_pk_add_f32 v[140:141], v[140:141], v[142:143]
	v_pk_add_f32 v[90:91], v[138:139], v[90:91]
	v_lshl_add_u64 v[142:143], s[10:11], 0, v[98:99]
	v_pk_add_f32 v[90:91], v[140:141], v[90:91]
	v_lshl_add_u64 v[98:99], v[98:99], 0, s[14:15]
	v_add_f32_e32 v81, v90, v91
	ds_bpermute_b32 v87, v126, v81
	v_mov_b32_e32 v91, v124
	v_mov_b32_e32 v124, v123
	v_mov_b32_e32 v90, v122
	v_mov_b32_e32 v122, v118
	s_waitcnt lgkmcnt(0)
; DI unsigned f2bf(float f) { unsigned u = __builtin_bit_cast(unsigned, f); return (u + 0x7fffu + ((u >> 16) & 1u)) >> 16; }
; template <bool ROUTE, bool COMBINE> ...
;     ...
;     const float rstd = 1.0f / sqrtf(wave_sum(s2) * (1.0f / D_) + LN_EPS);
;     float lg0 = 0.f, lg1 = 0.f, lg2 = 0.f, lg3 = 0.f, lg4 = 0.f, lg5 = 0.f, lg6 = 0.f, lg7 = 0.f;
; #pragma unroll
;     for (int j = 0; j < 4; ++j) {
;         const int c = 8 * lane + 512 * j;
;         const f32x4 oa = v[2 * j] * rstd * *(const f32x4*)(g + c) + *(const f32x4*)(bta + c), ob = v[2 * j + 1] * rstd * *(const f32x4*)(g + c + 4) + *(const f32x4*)(bta + c + 4);
;         if (X) { *(f32x4*)(X + (size_t)row * D_ + c) = oa; *(f32x4*)(X + (size_t)row * D_ + c + 4) = ob; }
;         if (XB) { u32x4 w; w.x = f2bf(oa.x) | (f2bf(oa.y) << 16); w.y = f2bf(oa.z) | (f2bf(oa.w) << 16); w.z = f2bf(ob.x) | (f2bf(ob.y) << 16); w.w = f2bf(ob.z) | (f2bf(ob.w) << 16);
;             *(u32x4*)(XB + (size_t)row * D_ + c) = w; }
;         if (XB8) { const f32x4 sa = oa * 16.f, sb = ob * 16.f;
;             int w0 = __builtin_amdgcn_cvt_pk_fp8_f32(__builtin_amdgcn_fmed3f(sa.x, -448.f, 448.f), __builtin_amdgcn_fmed3f(sa.y, -448.f, 448.f), 0, false);
;             w0 = __builtin_amdgcn_cvt_pk_fp8_f32(__builtin_amdgcn_fmed3f(sa.z, -448.f, 448.f), __builtin_amdgcn_fmed3f(sa.w, -448.f, 448.f), w0, true);
;             int w1 = __builtin_amdgcn_cvt_pk_fp8_f32(__builtin_amdgcn_fmed3f(sb.x, -448.f, 448.f), __builtin_amdgcn_fmed3f(sb.y, -448.f, 448.f), 0, false);
;             w1 = __builtin_amdgcn_cvt_pk_fp8_f32(__builtin_amdgcn_fmed3f(sb.z, -448.f, 448.f), __builtin_amdgcn_fmed3f(sb.w, -448.f, 448.f), w1, true);
;             *(u32x2*)(XB8 + (size_t)row * D_ + c) = (u32x2){(unsigned)w0, (unsigned)w1}; }
	v_add_f32_e32 v81, v81, v87
	ds_bpermute_b32 v87, v127, v81
	v_mov_b32_e32 v123, v120
	v_mov_b32_e32 v120, v119
	s_waitcnt lgkmcnt(0)
	v_add_f32_e32 v81, v81, v87
	ds_bpermute_b32 v87, v128, v81
	s_waitcnt lgkmcnt(0)
	v_add_f32_e32 v81, v81, v87
	ds_bpermute_b32 v87, v129, v81
	s_waitcnt lgkmcnt(0)
	v_add_f32_e32 v81, v81, v87
	ds_bpermute_b32 v87, v130, v81
	s_waitcnt lgkmcnt(0)
	v_add_f32_e32 v81, v81, v87
	ds_bpermute_b32 v87, v131, v81
	s_waitcnt lgkmcnt(0)
	v_add_f32_e32 v81, v81, v87
	v_fmamk_f32 v81, v81, 0x3a000000, v132
	v_mul_f32_e32 v87, 0x4f800000, v81
	v_cmp_gt_f32_e32 vcc, s9, v81
	s_nop 1
	v_cndmask_b32_e32 v81, v81, v87, vcc
	v_sqrt_f32_e32 v87, v81
	s_nop 0
	v_add_u32_e32 v93, -1, v87
	v_fma_f32 v95, -v93, v87, v81
	v_cmp_ge_f32_e64 s[4:5], 0, v95
	v_add_u32_e32 v95, 1, v87
	s_nop 0
	v_cndmask_b32_e64 v93, v87, v93, s[4:5]
	v_fma_f32 v87, -v95, v87, v81
	v_cmp_lt_f32_e64 s[4:5], 0, v87
	s_nop 1
	v_cndmask_b32_e64 v87, v93, v95, s[4:5]
	v_mul_f32_e32 v93, 0x37800000, v87
	v_cndmask_b32_e32 v87, v87, v93, vcc
	v_cmp_class_f32_e32 vcc, v81, v133
	s_nop 1
	v_cndmask_b32_e32 v81, v87, v81, vcc
	v_div_scale_f32 v87, s[4:5], v81, v81, 1.0
	v_rcp_f32_e32 v93, v87
	s_nop 0
	v_fma_f32 v95, -v87, v93, 1.0
	v_fmac_f32_e32 v93, v95, v93
	v_div_scale_f32 v95, vcc, 1.0, v81, 1.0
	v_mul_f32_e32 v107, v95, v93
	v_fma_f32 v109, -v87, v107, v95
	v_fmac_f32_e32 v107, v109, v93
	v_fma_f32 v87, -v87, v107, v95
	v_div_fmas_f32 v87, v87, v93, v107
	v_div_fixup_f32 v138, v87, v81, 1.0
	v_pk_mul_f32 v[118:119], v[124:125], v[138:139] op_sel_hi:[1,0]
	v_pk_mul_f32 v[120:121], v[120:121], v[138:139] op_sel_hi:[1,0]
	s_waitcnt vmcnt(12)
	v_pk_fma_f32 v[140:141], v[8:9], v[118:119], v[16:17]
	v_pk_fma_f32 v[124:125], v[10:11], v[120:121], v[18:19]
	v_pk_mul_f32 v[118:119], v[122:123], v[138:139] op_sel_hi:[1,0]
	v_pk_fma_f32 v[122:123], v[6:7], v[118:119], v[14:15]
	v_cvt_pk_bf16_f32 v118, v140, v141
	v_pk_mul_f32 v[90:91], v[90:91], v[138:139] op_sel_hi:[1,0]
	v_pk_fma_f32 v[90:91], v[4:5], v[90:91], v[12:13]
	v_cvt_pk_bf16_f32 v119, v124, v125
	v_cvt_pk_bf16_f32 v120, v90, v91
	v_add_co_u32_e32 v142, vcc, s20, v142
	v_cvt_pk_bf16_f32 v121, v122, v123
	s_nop 0
	v_addc_co_u32_e32 v143, vcc, 0, v143, vcc
	global_store_dwordx4 v[142:143], v[118:121], off
	v_pk_mul_f32 v[90:91], v[90:91], s[16:17] op_sel_hi:[1,0]
	v_pk_mul_f32 v[122:123], v[122:123], s[16:17] op_sel_hi:[1,0]
	v_pk_mul_f32 v[120:121], v[140:141], s[16:17] op_sel_hi:[1,0]
	v_med3_f32 v90, v90, s21, v134
	v_med3_f32 v81, v120, s21, v134
	v_med3_f32 v87, v121, s21, v134
	v_mov_b32_e32 v120, 0
	v_cvt_pk_fp8_f32 v120, v81, v87
	v_med3_f32 v91, v91, s21, v134
	v_mov_b32_e32 v121, 0
	v_cvt_pk_fp8_f32 v121, v90, v91
	v_pk_mul_f32 v[118:119], v[124:125], s[16:17] op_sel_hi:[1,0]
	v_pk_mul_f32 v[88:89], v[88:89], v[138:139] op_sel_hi:[1,0]
	v_med3_f32 v81, v118, s21, v134
	v_med3_f32 v87, v119, s21, v134
	v_cvt_pk_fp8_f32 v120, v81, v87 op_sel:[0,0,1]
	v_med3_f32 v81, v122, s21, v134
	v_med3_f32 v87, v123, s21, v134
	v_cvt_pk_fp8_f32 v121, v81, v87 op_sel:[0,0,1]
	v_lshl_add_u64 v[90:91], s[10:11], 0, v[96:97]
	s_waitcnt vmcnt(9)
	v_pk_fma_f32 v[122:123], v[24:25], v[88:89], v[32:33]
	v_add_co_u32_e32 v118, vcc, s22, v90
	s_nop 0
	v_addc_co_u32_e32 v119, vcc, 0, v91, vcc
	v_pk_mul_f32 v[90:91], v[136:137], v[138:139] op_sel_hi:[1,0]
	global_store_dwordx2 v[118:119], v[120:121], off
	v_pk_fma_f32 v[120:121], v[26:27], v[90:91], v[34:35]
	v_pk_mul_f32 v[88:89], v[114:115], v[138:139] op_sel_hi:[1,0]
	v_pk_mul_f32 v[90:91], v[116:117], v[138:139] op_sel_hi:[1,0]
	v_pk_fma_f32 v[116:117], v[20:21], v[88:89], v[28:29]
	v_cvt_pk_bf16_f32 v88, v122, v123
	v_cvt_pk_bf16_f32 v89, v120, v121
	v_bfe_u32 v81, v116, 16, 1
	v_bfe_u32 v87, v117, 16, 1
	v_pk_mul_f32 v[122:123], v[122:123], s[16:17] op_sel_hi:[1,0]
	v_pk_fma_f32 v[114:115], v[22:23], v[90:91], v[30:31]
	v_add3_u32 v81, v116, v81, s17
	v_add3_u32 v87, v117, v87, s17
	v_pk_mul_f32 v[116:117], v[116:117], s[16:17] op_sel_hi:[1,0]
	v_med3_f32 v91, v122, s21, v134
	v_med3_f32 v93, v123, s21, v134
	v_mov_b32_e32 v122, 0
	v_cvt_pk_fp8_f32 v122, v91, v93
	v_med3_f32 v95, v116, s21, v134
	v_med3_f32 v107, v117, s21, v134
	v_mov_b32_e32 v123, 0
	v_cvt_pk_fp8_f32 v123, v95, v107
	v_pk_mul_f32 v[120:121], v[120:121], s[16:17] op_sel_hi:[1,0]
	v_lshrrev_b32_e32 v81, 16, v81
	v_pk_mul_f32 v[124:125], v[114:115], s[16:17] op_sel_hi:[1,0]
	v_med3_f32 v91, v120, s21, v134
	v_med3_f32 v93, v121, s21, v134
	v_and_or_b32 v90, v87, s3, v81
	v_cvt_pk_fp8_f32 v122, v91, v93 op_sel:[0,0,1]
	v_med3_f32 v91, v124, s21, v134
	v_med3_f32 v93, v125, s21, v134
	v_cvt_pk_fp8_f32 v123, v91, v93 op_sel:[0,0,1]
	v_cvt_pk_bf16_f32 v91, v114, v115
	v_mov_b32_e32 v109, v112
	global_store_dwordx4 v[142:143], v[88:91], off offset:1024
	global_store_dwordx2 v[118:119], v[122:123], off offset:512
	v_mov_b32_e32 v107, v110
	v_pk_mul_f32 v[88:89], v[108:109], v[138:139] op_sel_hi:[1,0]
	v_pk_mul_f32 v[82:83], v[82:83], v[138:139] op_sel_hi:[1,0]
	s_waitcnt vmcnt(8)
; DI unsigned f2bf(float f) { unsigned u = __builtin_bit_cast(unsigned, f); return (u + 0x7fffu + ((u >> 16) & 1u)) >> 16; }
; template <bool ROUTE, bool COMBINE> ...
;     ...
;     for (int j = 0; j < 4; ++j) {
;         const int c = 8 * lane + 512 * j;
;         const f32x4 oa = v[2 * j] * rstd * *(const f32x4*)(g + c) + *(const f32x4*)(bta + c), ob = v[2 * j + 1] * rstd * *(const f32x4*)(g + c + 4) + *(const f32x4*)(bta + c + 4);
;         if (X) { *(f32x4*)(X + (size_t)row * D_ + c) = oa; *(f32x4*)(X + (size_t)row * D_ + c + 4) = ob; }
;         if (XB) { u32x4 w; w.x = f2bf(oa.x) | (f2bf(oa.y) << 16); w.y = f2bf(oa.z) | (f2bf(oa.w) << 16); w.z = f2bf(ob.x) | (f2bf(ob.y) << 16); w.w = f2bf(ob.z) | (f2bf(ob.w) << 16);
;             *(u32x4*)(XB + (size_t)row * D_ + c) = w; }
;         if (XB8) { const f32x4 sa = oa * 16.f, sb = ob * 16.f;
;             int w0 = __builtin_amdgcn_cvt_pk_fp8_f32(__builtin_amdgcn_fmed3f(sa.x, -448.f, 448.f), __builtin_amdgcn_fmed3f(sa.y, -448.f, 448.f), 0, false);
;             w0 = __builtin_amdgcn_cvt_pk_fp8_f32(__builtin_amdgcn_fmed3f(sa.z, -448.f, 448.f), __builtin_amdgcn_fmed3f(sa.w, -448.f, 448.f), w0, true);
;             int w1 = __builtin_amdgcn_cvt_pk_fp8_f32(__builtin_amdgcn_fmed3f(sb.x, -448.f, 448.f), __builtin_amdgcn_fmed3f(sb.y, -448.f, 448.f), 0, false);
;             w1 = __builtin_amdgcn_cvt_pk_fp8_f32(__builtin_amdgcn_fmed3f(sb.z, -448.f, 448.f), __builtin_amdgcn_fmed3f(sb.w, -448.f, 448.f), w1, true);
;             *(u32x2*)(XB8 + (size_t)row * D_ + c) = (u32x2){(unsigned)w0, (unsigned)w1}; }
	v_pk_fma_f32 v[88:89], v[40:41], v[88:89], v[48:49]
	v_pk_mul_f32 v[90:91], v[106:107], v[138:139] op_sel_hi:[1,0]
	v_pk_fma_f32 v[106:107], v[38:39], v[82:83], v[46:47]
	v_pk_fma_f32 v[90:91], v[42:43], v[90:91], v[50:51]
	v_cvt_pk_bf16_f32 v82, v88, v89
	v_pk_mul_f32 v[84:85], v[84:85], v[138:139] op_sel_hi:[1,0]
	v_pk_fma_f32 v[108:109], v[36:37], v[84:85], v[44:45]
	v_cvt_pk_bf16_f32 v83, v90, v91
	v_bfe_u32 v81, v108, 16, 1
	v_bfe_u32 v84, v109, 16, 1
	v_pk_mul_f32 v[88:89], v[88:89], s[16:17] op_sel_hi:[1,0]
	v_add3_u32 v81, v108, v81, s17
	v_add3_u32 v84, v109, v84, s17
	v_pk_mul_f32 v[90:91], v[90:91], s[16:17] op_sel_hi:[1,0]
	v_pk_mul_f32 v[108:109], v[108:109], s[16:17] op_sel_hi:[1,0]
	v_med3_f32 v87, v88, s21, v134
	v_med3_f32 v89, v89, s21, v134
	v_mov_b32_e32 v88, 0
	v_cvt_pk_fp8_f32 v88, v87, v89
	v_med3_f32 v87, v90, s21, v134
	v_med3_f32 v90, v91, s21, v134
	v_med3_f32 v91, v108, s21, v134
	v_med3_f32 v93, v109, s21, v134
	v_mov_b32_e32 v89, 0
	v_cvt_pk_fp8_f32 v89, v91, v93
	v_lshrrev_b32_e32 v81, 16, v81
	v_pk_mul_f32 v[110:111], v[106:107], s[16:17] op_sel_hi:[1,0]
	v_and_or_b32 v84, v84, s3, v81
	v_cvt_pk_fp8_f32 v88, v87, v90 op_sel:[0,0,1]
	v_med3_f32 v87, v110, s21, v134
	v_med3_f32 v90, v111, s21, v134
	v_cvt_pk_fp8_f32 v89, v87, v90 op_sel:[0,0,1]
	v_cvt_pk_bf16_f32 v85, v106, v107
	global_store_dwordx4 v[142:143], v[82:85], off offset:2048
	global_store_dwordx2 v[118:119], v[88:89], off offset:1024
	v_mov_b32_e32 v81, v92
	v_pk_mul_f32 v[82:83], v[102:103], v[138:139] op_sel_hi:[1,0]
	v_mov_b32_e32 v87, v94
	s_waitcnt vmcnt(6)
	v_pk_fma_f32 v[88:89], v[56:57], v[82:83], v[64:65]
	v_pk_mul_f32 v[80:81], v[80:81], v[138:139] op_sel_hi:[1,0]
	v_pk_mul_f32 v[82:83], v[86:87], v[138:139] op_sel_hi:[1,0]
	v_pk_fma_f32 v[86:87], v[54:55], v[80:81], v[62:63]
	v_pk_mul_f32 v[84:85], v[104:105], v[138:139] op_sel_hi:[1,0]
	v_pk_fma_f32 v[84:85], v[58:59], v[84:85], v[66:67]
	v_cvt_pk_bf16_f32 v80, v88, v89
	v_pk_fma_f32 v[90:91], v[52:53], v[82:83], v[60:61]
	v_cvt_pk_bf16_f32 v81, v84, v85
	v_cvt_pk_bf16_f32 v82, v90, v91
	v_bfe_u32 v83, v86, 16, 1
	v_pk_mul_f32 v[88:89], v[88:89], s[16:17] op_sel_hi:[1,0]
	v_add3_u32 v83, v86, v83, s17
	v_pk_mul_f32 v[92:93], v[86:87], s[16:17] op_sel_hi:[1,0]
	v_pk_mul_f32 v[90:91], v[90:91], s[16:17] op_sel_hi:[1,0]
	v_med3_f32 v86, v88, s21, v134
	v_med3_f32 v89, v89, s21, v134
	v_mov_b32_e32 v88, 0
	v_cvt_pk_fp8_f32 v88, v86, v89
	v_med3_f32 v86, v90, s21, v134
	v_med3_f32 v90, v91, s21, v134
	v_mov_b32_e32 v89, 0
	v_cvt_pk_fp8_f32 v89, v86, v90
	v_pk_mul_f32 v[84:85], v[84:85], s[16:17] op_sel_hi:[1,0]
	v_bfe_u32 v94, v87, 16, 1
	v_med3_f32 v84, v84, s21, v134
	v_med3_f32 v85, v85, s21, v134
	v_cvt_pk_fp8_f32 v88, v84, v85 op_sel:[0,0,1]
	v_med3_f32 v84, v92, s21, v134
	v_med3_f32 v85, v93, s21, v134
	v_cvt_pk_fp8_f32 v89, v84, v85 op_sel:[0,0,1]
	v_lshrrev_b32_e32 v83, 16, v83
	v_add3_u32 v84, v87, v94, s17
	v_and_or_b32 v83, v84, s3, v83
	global_store_dwordx4 v[142:143], v[80:83], off offset:3072
	global_store_dwordx2 v[118:119], v[88:89], off offset:1536
	v_lshl_add_u64 v[96:97], v[96:97], 0, s[12:13]
	s_andn2_b64 vcc, exec, s[18:19]
	v_mov_b32_e32 v92, v76
	v_mov_b32_e32 v93, v77
	v_mov_b32_e32 v94, v78
	v_mov_b32_e32 v95, v79
	v_mov_b32_e32 v80, v72
	v_mov_b32_e32 v81, v73
	v_mov_b32_e32 v82, v74
	v_mov_b32_e32 v83, v75
	v_mov_b32_e32 v84, v68
	v_mov_b32_e32 v85, v69
	v_mov_b32_e32 v86, v70
	v_mov_b32_e32 v87, v71
	v_mov_b32_e32 v88, v0
	v_mov_b32_e32 v89, v1
	v_mov_b32_e32 v90, v2
	v_mov_b32_e32 v91, v3
	s_cbranch_vccz .LBB0_876

; template <bool ROUTE, bool COMBINE> ...
;     f32x4 v[8]; float s = 0.f;
;     if (!COMBINE) {
;         if (pre) {
; #pragma unroll
;             for (int j = 0; j < 4; ++j) bf8_to_f32(pre[j], v[2 * j], v[2 * j + 1]);
;         } else {
;             const bf16* yr = Yb + (size_t)row * D_ + 8 * lane;
; #pragma unroll
;             for (int j = 0; j < 4; ++j) bf8_to_f32(*(const u32x4*)(yr + 512 * j), v[2 * j], v[2 * j + 1]);
;         }
;     } else {
;         const int p0 = pos[row * 2], p1 = pos[row * 2 + 1]; const float g0 = topg[row * 2], g1 = topg[row * 2 + 1];
; #pragma unroll
;         for (int j = 0; j < 4; ++j) { const int c = 8 * lane + 512 * j;
;             f32x4 xa, xb, pa, pb, a0, a1, c0, c1;
;             bf8_to_f32(*(const u32x4*)(X1B + (size_t)row * D_ + c), xa, xb); bf8_to_f32(*(const u32x4*)(PLEB + (size_t)row * D_ + c), pa, pb);
;             bf8_to_f32(*(const u32x4*)(YE + (size_t)p0 * D_ + c), a0, a1);
;             bf8_to_f32(*(const u32x4*)(YE + (size_t)p1 * D_ + c), c0, c1);
;             v[2 * j] = (ALPHA * xa + (g0 * a0 + g1 * c0)) + pa; v[2 * j + 1] = (ALPHA * xb + (g0 * a1 + g1 * c1)) + pb; }
;     }
; #pragma unroll
;     for (int j = 0; j < 8; ++j) s += (v[j].x + v[j].y) + (v[j].z + v[j].w);
;     const float mean = wave_sum(s) * (1.0f / D_); float s2 = 0.f;
; #pragma unroll
;     for (int j = 0; j < 8; ++j) { v[j] = v[j] - mean; s2 += (v[j].x * v[j].x + v[j].y * v[j].y) + (v[j].z * v[j].z + v[j].w * v[j].w); }
;     const float rstd = 1.0f / sqrtf(wave_sum(s2) * (1.0f / D_) + LN_EPS);
.LBB0_1377:
	s_waitcnt vmcnt(18)
	v_lshlrev_b32_e32 v112, 16, v86
	v_and_b32_e32 v113, 0xffff0000, v86
	v_lshlrev_b32_e32 v114, 16, v87
	v_and_b32_e32 v115, 0xffff0000, v87
	v_lshlrev_b32_e32 v111, 16, v88
	v_lshlrev_b32_e32 v110, 16, v90
	v_and_b32_e32 v127, 0xffff0000, v88
	v_and_b32_e32 v126, 0xffff0000, v90
	v_lshlrev_b32_e32 v87, 16, v89
	v_lshlrev_b32_e32 v86, 16, v91
	v_and_b32_e32 v89, 0xffff0000, v89
	v_and_b32_e32 v88, 0xffff0000, v91
	s_waitcnt vmcnt(17)
	v_lshlrev_b32_e32 v118, 16, v80
	v_and_b32_e32 v122, 0xffff0000, v80
	v_lshlrev_b32_e32 v116, 16, v81
	v_and_b32_e32 v120, 0xffff0000, v81
	v_pk_add_f32 v[80:81], v[110:111], v[126:127]
	v_pk_add_f32 v[90:91], v[86:87], v[88:89]
	v_add_f32_e32 v119, v112, v113
	v_pk_add_f32 v[80:81], v[80:81], v[90:91]
	v_lshlrev_b32_e32 v91, 16, v85
	v_add_f32_e32 v81, 0, v81
	v_add_f32_e32 v121, v80, v81
	v_lshlrev_b32_e32 v90, 16, v84
	v_and_b32_e32 v81, 0xffff0000, v85
	v_and_b32_e32 v80, 0xffff0000, v84
	v_pk_add_f32 v[84:85], v[90:91], v[80:81]
	v_add_f32_e32 v123, v114, v115
	v_pk_add_f32 v[84:85], v[84:85], v[84:85] op_sel_hi:[0,1]
	v_mov_b32_e32 v117, v85
	v_pk_add_f32 v[124:125], v[118:119], v[122:123]
	v_pk_add_f32 v[84:85], v[116:117], v[120:121]
	s_waitcnt vmcnt(16)
	v_lshlrev_b32_e32 v106, 16, v92
	v_pk_add_f32 v[84:85], v[124:125], v[84:85]
	v_lshlrev_b32_e32 v125, 16, v83
	v_lshlrev_b32_e32 v124, 16, v82
	v_and_b32_e32 v83, 0xffff0000, v83
	v_and_b32_e32 v82, 0xffff0000, v82
	v_pk_add_f32 v[138:139], v[124:125], v[82:83]
	v_and_b32_e32 v107, 0xffff0000, v92
	v_lshlrev_b32_e32 v108, 16, v93
	v_and_b32_e32 v109, 0xffff0000, v93
	v_pk_add_f32 v[84:85], v[84:85], v[84:85] op_sel_hi:[0,1]
	v_pk_add_f32 v[138:139], v[138:139], v[138:139] op_sel_hi:[0,1]
	v_lshlrev_b32_e32 v102, 16, v94
	v_and_b32_e32 v104, 0xffff0000, v94
	v_lshlrev_b32_e32 v92, 16, v95
	v_and_b32_e32 v94, 0xffff0000, v95
	v_add_f32_e32 v103, v106, v107
	v_add_f32_e32 v105, v108, v109
	v_mov_b32_e32 v93, v139
	v_mov_b32_e32 v95, v85
	v_pk_add_f32 v[140:141], v[102:103], v[104:105]
	v_pk_add_f32 v[84:85], v[92:93], v[94:95]
	s_ashr_i32 s17, s16, 31
	v_pk_add_f32 v[84:85], v[140:141], v[84:85]
	s_lshl_b64 s[8:9], s[16:17], 12
	v_add_f32_e32 v84, v84, v85
	ds_bpermute_b32 v85, v129, v84
	v_lshl_add_u64 v[148:149], v[100:101], 0, s[8:9]
	s_waitcnt lgkmcnt(0)
	v_add_f32_e32 v84, v84, v85
	ds_bpermute_b32 v85, v130, v84
	s_waitcnt lgkmcnt(0)
	v_add_f32_e32 v84, v84, v85
	ds_bpermute_b32 v85, v131, v84
	s_waitcnt lgkmcnt(0)
	v_add_f32_e32 v84, v84, v85
	ds_bpermute_b32 v85, v132, v84
	s_waitcnt lgkmcnt(0)
	v_add_f32_e32 v84, v84, v85
	ds_bpermute_b32 v85, v133, v84
	s_waitcnt lgkmcnt(0)
	v_add_f32_e32 v84, v84, v85
	ds_bpermute_b32 v85, v134, v84
	s_waitcnt lgkmcnt(0)
	v_add_f32_e32 v93, v84, v85
	v_fmac_f32_e32 v127, 0xba000000, v93
	v_fmac_f32_e32 v126, 0xba000000, v93
	v_fmac_f32_e32 v89, 0xba000000, v93
	v_fmac_f32_e32 v111, 0xba000000, v93
	v_fmac_f32_e32 v88, 0xba000000, v93
	v_fmac_f32_e32 v110, 0xba000000, v93
	v_mov_b32_e32 v138, v127
	v_mov_b32_e32 v139, v126
	v_fmac_f32_e32 v87, 0xba000000, v93
	v_fmac_f32_e32 v86, 0xba000000, v93
	v_mov_b32_e32 v84, v111
	v_mov_b32_e32 v85, v110
	v_pk_mul_f32 v[138:139], v[138:139], v[138:139]
	v_mov_b32_e32 v140, v89
	v_mov_b32_e32 v141, v88
	v_pk_fma_f32 v[84:85], v[84:85], v[84:85], v[138:139]
	v_mov_b32_e32 v138, v87
	v_mov_b32_e32 v139, v86
	v_pk_mul_f32 v[140:141], v[140:141], v[140:141]
	v_fmac_f32_e32 v80, 0xba000000, v93
	v_fmac_f32_e32 v81, 0xba000000, v93
	v_fmac_f32_e32 v91, 0xba000000, v93
	v_pk_fma_f32 v[138:139], v[138:139], v[138:139], v[140:141]
	v_fmac_f32_e32 v90, 0xba000000, v93
	v_mov_b32_e32 v142, v91
	v_mov_b32_e32 v143, v81
	v_mov_b32_e32 v91, v80
	v_pk_add_f32 v[84:85], v[84:85], v[138:139]
	v_pk_mul_f32 v[138:139], v[142:143], v[142:143]
	v_pk_mul_f32 v[80:81], v[90:91], v[90:91]
	v_fmac_f32_e32 v112, 0xba000000, v93
	v_pk_mov_b32 v[140:141], v[80:81], v[138:139] op_sel:[1,0]
	v_mov_b32_e32 v81, v139
	v_pk_add_f32 v[80:81], v[140:141], v[80:81]
	v_fmac_f32_e32 v113, 0xba000000, v93
	v_pk_add_f32 v[80:81], v[80:81], v[80:81] op_sel_hi:[0,1]
	v_fmac_f32_e32 v114, 0xba000000, v93
	v_mul_f32_e32 v80, v112, v112
	v_fmac_f32_e32 v115, 0xba000000, v93
	v_pk_fma_f32 v[138:139], v[112:113], v[112:113], v[80:81] op_sel_hi:[1,1,0]
	v_mul_f32_e32 v80, v114, v114
	v_pk_add_f32 v[84:85], v[84:85], v[84:85] op_sel_hi:[0,1]
	v_pk_fma_f32 v[140:141], v[114:115], v[114:115], v[80:81] op_sel_hi:[1,1,0]
	v_fmac_f32_e32 v120, 0xba000000, v93
	v_fmac_f32_e32 v116, 0xba000000, v93
	v_fmac_f32_e32 v122, 0xba000000, v93
	v_fmac_f32_e32 v118, 0xba000000, v93
	v_mul_f32_e32 v138, v118, v118
	v_mul_f32_e32 v140, v122, v122
	v_mul_f32_e32 v80, v116, v116
	v_mul_f32_e32 v84, v120, v120
	v_pk_add_f32 v[138:139], v[138:139], v[140:141]
	v_pk_add_f32 v[80:81], v[80:81], v[84:85]
	v_fmac_f32_e32 v82, 0xba000000, v93
	v_fmac_f32_e32 v83, 0xba000000, v93
	v_fmac_f32_e32 v125, 0xba000000, v93
	v_pk_add_f32 v[80:81], v[138:139], v[80:81]
	v_fmac_f32_e32 v124, 0xba000000, v93
	v_mov_b32_e32 v144, v125
	v_mov_b32_e32 v145, v83
	v_mov_b32_e32 v125, v82
	v_pk_add_f32 v[80:81], v[80:81], v[80:81] op_sel_hi:[0,1]
	v_pk_mul_f32 v[84:85], v[144:145], v[144:145]
	v_pk_mul_f32 v[82:83], v[124:125], v[124:125]
	v_fmac_f32_e32 v106, 0xba000000, v93
	v_pk_mov_b32 v[138:139], v[82:83], v[84:85] op_sel:[1,0]
	v_mov_b32_e32 v83, v85
	v_fmac_f32_e32 v107, 0xba000000, v93
	v_fmac_f32_e32 v108, 0xba000000, v93
	v_mul_f32_e32 v80, v106, v106
	v_pk_add_f32 v[82:83], v[138:139], v[82:83]
	v_fmac_f32_e32 v109, 0xba000000, v93
	v_pk_fma_f32 v[84:85], v[106:107], v[106:107], v[80:81] op_sel_hi:[1,1,0]
	v_mul_f32_e32 v80, v108, v108
	v_pk_add_f32 v[82:83], v[82:83], v[82:83] op_sel_hi:[0,1]
	v_pk_fma_f32 v[138:139], v[108:109], v[108:109], v[80:81] op_sel_hi:[1,1,0]
	v_fmac_f32_e32 v94, 0xba000000, v93
	v_fmac_f32_e32 v92, 0xba000000, v93
	v_fmac_f32_e32 v104, 0xba000000, v93
	v_fmac_f32_e32 v102, 0xba000000, v93
	v_mul_f32_e32 v84, v102, v102
	v_mul_f32_e32 v138, v104, v104
	v_mul_f32_e32 v82, v92, v92
	v_mul_f32_e32 v80, v94, v94
	v_pk_add_f32 v[84:85], v[84:85], v[138:139]
	v_pk_add_f32 v[80:81], v[82:83], v[80:81]
	v_mov_b32_e32 v138, v110
	v_pk_add_f32 v[80:81], v[84:85], v[80:81]
	v_mov_b32_e32 v110, v86
	v_add_f32_e32 v80, v80, v81
	ds_bpermute_b32 v81, v129, v80
	v_mov_b32_e32 v139, v126
	v_mov_b32_e32 v126, v111
	v_mov_b32_e32 v111, v88
	v_mov_b32_e32 v88, v87
	s_waitcnt lgkmcnt(0)
; DI unsigned f2bf(float f) { unsigned u = __builtin_bit_cast(unsigned, f); return (u + 0x7fffu + ((u >> 16) & 1u)) >> 16; }
; template <bool ROUTE, bool COMBINE> ...
;     ...
;     const float rstd = 1.0f / sqrtf(wave_sum(s2) * (1.0f / D_) + LN_EPS);
;     float lg0 = 0.f, lg1 = 0.f, lg2 = 0.f, lg3 = 0.f, lg4 = 0.f, lg5 = 0.f, lg6 = 0.f, lg7 = 0.f;
; #pragma unroll
;     for (int j = 0; j < 4; ++j) {
;         const int c = 8 * lane + 512 * j;
;         const f32x4 oa = v[2 * j] * rstd * *(const f32x4*)(g + c) + *(const f32x4*)(bta + c), ob = v[2 * j + 1] * rstd * *(const f32x4*)(g + c + 4) + *(const f32x4*)(bta + c + 4);
;         if (X) { *(f32x4*)(X + (size_t)row * D_ + c) = oa; *(f32x4*)(X + (size_t)row * D_ + c + 4) = ob; }
;         if (XB) { u32x4 w; w.x = f2bf(oa.x) | (f2bf(oa.y) << 16); w.y = f2bf(oa.z) | (f2bf(oa.w) << 16); w.z = f2bf(ob.x) | (f2bf(ob.y) << 16); w.w = f2bf(ob.z) | (f2bf(ob.w) << 16);
;             *(u32x4*)(XB + (size_t)row * D_ + c) = w; }
	v_add_f32_e32 v80, v80, v81
	ds_bpermute_b32 v81, v130, v80
	v_mov_b32_e32 v119, v122
	v_mov_b32_e32 v117, v120
	v_mov_b32_e32 v103, v104
	s_waitcnt lgkmcnt(0)
	v_add_f32_e32 v80, v80, v81
	ds_bpermute_b32 v81, v131, v80
	s_waitcnt lgkmcnt(0)
	v_add_f32_e32 v80, v80, v81
	ds_bpermute_b32 v81, v132, v80
	s_waitcnt lgkmcnt(0)
	v_add_f32_e32 v80, v80, v81
	ds_bpermute_b32 v81, v133, v80
	s_waitcnt lgkmcnt(0)
	v_add_f32_e32 v81, v80, v81
	ds_bpermute_b32 v82, v134, v81
	v_mov_b32_e32 v80, 0
	s_waitcnt lgkmcnt(0)
	v_add_f32_e32 v81, v81, v82
	v_fmamk_f32 v81, v81, 0x3a000000, v96
	v_mul_f32_e32 v82, 0x4f800000, v81
	v_cmp_gt_f32_e32 vcc, s28, v81
	s_nop 1
	v_cndmask_b32_e32 v81, v81, v82, vcc
	v_sqrt_f32_e32 v82, v81
	s_nop 0
	v_add_u32_e32 v83, -1, v82
	v_fma_f32 v84, -v83, v82, v81
	v_cmp_ge_f32_e64 s[6:7], 0, v84
	v_add_u32_e32 v84, 1, v82
	s_nop 0
	v_cndmask_b32_e64 v83, v82, v83, s[6:7]
	v_fma_f32 v82, -v84, v82, v81
	v_cmp_lt_f32_e64 s[6:7], 0, v82
	s_nop 1
	v_cndmask_b32_e64 v82, v83, v84, s[6:7]
	v_mul_f32_e32 v83, 0x37800000, v82
	v_cndmask_b32_e32 v82, v82, v83, vcc
	v_cmp_class_f32_e32 vcc, v81, v135
	s_nop 1
	v_cndmask_b32_e32 v81, v82, v81, vcc
	v_div_scale_f32 v82, s[6:7], v81, v81, 1.0
	v_rcp_f32_e32 v83, v82
	s_mov_b32 s6, 0
	s_mov_b32 s7, 0
	v_fma_f32 v84, -v82, v83, 1.0
	v_fmac_f32_e32 v83, v84, v83
	v_div_scale_f32 v84, vcc, 1.0, v81, 1.0
	v_mul_f32_e32 v85, v84, v83
	v_fma_f32 v86, -v82, v85, v84
	v_fmac_f32_e32 v85, v86, v83
	v_fma_f32 v82, -v82, v85, v84
	v_div_fmas_f32 v82, v82, v83, v85
	v_div_fixup_f32 v146, v82, v81, 1.0
	v_pk_mul_f32 v[84:85], v[126:127], v[146:147] op_sel_hi:[1,0]
	v_pk_mul_f32 v[82:83], v[88:89], v[146:147] op_sel_hi:[1,0]
	s_waitcnt vmcnt(12)
	v_pk_fma_f32 v[84:85], v[4:5], v[84:85], v[12:13]
	v_pk_fma_f32 v[82:83], v[6:7], v[82:83], v[14:15]
	v_pk_mul_f32 v[88:89], v[138:139], v[146:147] op_sel_hi:[1,0]
	v_cvt_pk_bf16_f32 v138, v84, v85
	v_pk_fma_f32 v[88:89], v[0:1], v[88:89], v[8:9]
	v_cvt_pk_bf16_f32 v139, v82, v83
	v_pk_mul_f32 v[86:87], v[110:111], v[146:147] op_sel_hi:[1,0]
	v_pk_fma_f32 v[86:87], v[2:3], v[86:87], v[10:11]
	v_cvt_pk_bf16_f32 v140, v88, v89
	v_pk_mul_f32 v[110:111], v[90:91], v[146:147] op_sel_hi:[1,0]
	s_waitcnt vmcnt(8)
	v_pk_fma_f32 v[110:111], v[20:21], v[110:111], v[28:29]
	v_cvt_pk_bf16_f32 v141, v86, v87
	v_pk_mul_f32 v[90:91], v[142:143], v[146:147] op_sel_hi:[1,0]
	v_pk_fma_f32 v[90:91], v[22:23], v[90:91], v[30:31]
	global_store_dwordx4 v[148:149], v[138:141], off
	v_pk_mul_f32 v[126:127], v[112:113], v[146:147] op_sel_hi:[1,0]
	v_pk_mul_f32 v[112:113], v[114:115], v[146:147] op_sel_hi:[1,0]
	v_cvt_pk_bf16_f32 v138, v110, v111
	v_pk_fma_f32 v[114:115], v[16:17], v[126:127], v[24:25]
	v_cvt_pk_bf16_f32 v139, v90, v91
	v_pk_fma_f32 v[112:113], v[18:19], v[112:113], v[26:27]
	v_cvt_pk_bf16_f32 v140, v114, v115
	v_pk_mul_f32 v[118:119], v[118:119], v[146:147] op_sel_hi:[1,0]
	s_waitcnt vmcnt(5)
	v_pk_fma_f32 v[118:119], v[36:37], v[118:119], v[44:45]
	v_cvt_pk_bf16_f32 v141, v112, v113
	v_pk_mul_f32 v[116:117], v[116:117], v[146:147] op_sel_hi:[1,0]
	v_pk_fma_f32 v[116:117], v[38:39], v[116:117], v[46:47]
	v_pk_mul_f32 v[122:123], v[124:125], v[146:147] op_sel_hi:[1,0]
	v_cvt_pk_bf16_f32 v124, v118, v119
	v_pk_fma_f32 v[122:123], v[32:33], v[122:123], v[40:41]
	v_cvt_pk_bf16_f32 v125, v116, v117
	v_pk_mul_f32 v[120:121], v[144:145], v[146:147] op_sel_hi:[1,0]
	v_pk_fma_f32 v[120:121], v[34:35], v[120:121], v[42:43]
	v_cvt_pk_bf16_f32 v126, v122, v123
	v_cvt_pk_bf16_f32 v127, v120, v121
	global_store_dwordx4 v[148:149], v[124:127], off offset:2048
	v_mov_b32_e32 v93, v94
	v_pk_mul_f32 v[92:93], v[92:93], v[146:147] op_sel_hi:[1,0]
	v_pk_mul_f32 v[124:125], v[106:107], v[146:147] op_sel_hi:[1,0]
	v_pk_mul_f32 v[106:107], v[108:109], v[146:147] op_sel_hi:[1,0]
	s_waitcnt vmcnt(2)
	v_pk_fma_f32 v[108:109], v[52:53], v[124:125], v[60:61]
	v_pk_mul_f32 v[104:105], v[102:103], v[146:147] op_sel_hi:[1,0]
	v_pk_fma_f32 v[102:103], v[50:51], v[92:93], v[58:59]
	v_pk_fma_f32 v[106:107], v[54:55], v[106:107], v[62:63]
	v_cvt_pk_bf16_f32 v92, v108, v109
	v_pk_fma_f32 v[104:105], v[48:49], v[104:105], v[56:57]
	v_cvt_pk_bf16_f32 v93, v106, v107
	v_cvt_pk_bf16_f32 v94, v104, v105
	v_cvt_pk_bf16_f32 v95, v102, v103
	global_store_dwordx4 v[148:149], v[92:95], off offset:3072
	v_mov_b32_e32 v81, v80
	v_mov_b32_e32 v124, v80
	v_mov_b32_e32 v125, v80
	v_mov_b32_e32 v94, v80
	v_mov_b32_e32 v95, v80
	v_mov_b32_e32 v92, v80
	v_mov_b32_e32 v93, v80
	global_store_dwordx4 v[148:149], v[138:141], off offset:1024
